# P1: 72 converters, the 184 GEMM workgroups stop after 16 tiles; the last 128 in-projection tiles (gate_r columns) are computed in P3 by workgroups 128-255 while 0-127 run the chunk scan
# baseline (speedup 1.0000x reference)
; #define LAS __attribute__((address_space(3)))
; __global__ void __launch_bounds__(NTHREADS, 2) mk_fwd(Args args) {
;     extern __shared__ __attribute__((aligned(16))) unsigned char lds[];
;     Frame F;
;     F.lds = (LAS unsigned char*)lds;
;     F.tid = threadIdx.x; F.lane = F.tid & 63; F.wave = __builtin_amdgcn_readfirstlane(F.tid >> 6);
;     F.G = gridDim.x; { const int bx = blockIdx.x; F.vcu = (F.G % 8 == 0) ? (bx % 8) * (F.G / 8) + bx / 8 : bx; }
_Z6mk_fwd4Args:
	s_mov_b32 s92, s2
	s_mov_b32 s98, s2
	s_mov_b32 s101, 0
	s_load_dword s2, s[0:1], 0xc8
	s_mov_b64 s[96:97], s[0:1]
	s_add_u32 s0, s96, 0xc8
	s_addc_u32 s1, s97, 0
	v_writelane_b32 v254, s0, 0
	s_nop 1
	v_writelane_b32 v254, s1, 1
	s_waitcnt lgkmcnt(0)
	s_and_b32 s0, s2, 7
	s_cmp_lg_u32 s0, 0
	s_mov_b32 s0, s92
	v_writelane_b32 v254, s0, 2
	s_cbranch_scc1 .LBB0_2
	s_ashr_i32 s1, s92, 31
	s_lshr_b32 s1, s1, 29
	s_add_i32 s1, s92, s1
	s_and_b32 s3, s1, -8
	s_ashr_i32 s0, s2, 3
	s_sub_i32 s3, s92, s3
	s_mul_i32 s0, s0, s3
	s_ashr_i32 s1, s1, 3
	s_add_i32 s0, s0, s1
	v_writelane_b32 v254, s0, 2

; #define LAS __attribute__((address_space(3)))
; __device__ __forceinline__ void transpose_item(const float* W, int K, int N, bf16_t* WT, int mode, int item, LAS unsigned* scr, int lane) {
;     const int nblk = N / 32, kb = item / nblk, nb = item % nblk, k0 = 64 * kb, n0 = 32 * nb;
;     const int g = lane & 7, r = lane >> 3;
;     const int sc = src_col(mode, n0 + 4 * g);
;     const float* p = W + (size_t)(k0 + 2 * r) * N + sc;
;     f32x4 a[4], b[4];
; #pragma unroll
;     for (int i = 0; i < 4; ++i) { a[i] = *(const f32x4*)(p + (size_t)(16 * i) * N); b[i] = *(const f32x4*)(p + (size_t)(16 * i + 1) * N); }
; __global__ void __launch_bounds__(NTHREADS, 2) mk_fwd(Args args) {
;     ...
;         const int nconv = (MK_NCONV * F.G) / 256, ngemm = F.G - nconv;
;         if ((int)blockIdx.x < ngemm) {
;             pg8::DenseSched S; S.init((const bf16_t*)(F.ws + WS_H), D, (const bf16_t*)(F.ws + WS_WIN), D, T, INW, ngemm, (int)blockIdx.x);
;             EpiInProj E{F.ws};
;             if (MK_RSYNC) pg8::gemm_phase<0, EpiInProj, pg8::DenseSched, 127, 127, true>(F.lds, S, E, &bar); else pg8::gemm_phase<0>(F.lds, S, E);
;         } else if (!MK_CONV_IN_P0) conv_rest(F, args, ((int)blockIdx.x - ngemm) * NWAVES + F.wave, nconv * NWAVES);
.LBB0_102:
	s_cmp_lt_i32 s88, 2
	s_cselect_b64 s[4:5], -1, 0
	s_and_b64 s[14:15], s[4:5], s[0:1]
	s_andn2_b64 vcc, exec, s[14:15]
	s_cbranch_vccnz .LBB0_282
	s_ashr_i32 s0, s2, 31
	s_lshr_b32 s0, s0, 30
	s_add_i32 s0, s2, s0
	s_movk_i32 s18, 72
	s_waitcnt vmcnt(6)
	v_mov_b32_e32 v18, v0
	s_sub_i32 s3, s2, s18
	s_cmp_ge_i32 s92, s3
	v_readfirstlane_b32 s4, v18
	s_mov_b64 s[0:1], -1
	s_movk_i32 s99, 0xb80
	s_cbranch_scc0 .LBB0_126
	s_sub_i32 s0, s92, s3
	s_ashr_i32 s19, s4, 6
	s_lshl_b32 s0, s0, 3
	s_add_i32 s21, s19, s0
	s_mul_i32 s0, s19, 0x3600
	s_add_i32 s34, s0, 0
	s_load_dwordx2 s[8:9], s[96:97], 0x68
	s_load_dwordx2 s[0:1], s[96:97], 0x78
	s_waitcnt vmcnt(4)
	v_and_b32_e32 v2, 7, v18
	v_bfe_u32 v1, v18, 3, 3
	v_lshlrev_b32_e32 v164, 4, v2
	s_lshl_b32 s20, s18, 3
	v_lshl_add_u32 v3, v1, 2, s34
	v_mul_u32_u24_e32 v4, 0x210, v2
	v_mul_u32_u24_e32 v5, 0x84, v1
	s_waitcnt vmcnt(2)
	v_add_u32_e32 v6, s34, v164
	v_and_b32_e32 v19, 63, v18
	s_mov_b32 s11, 0
	v_or_b32_e32 v173, 8, v1
	v_or_b32_e32 v168, 16, v1
	v_or_b32_e32 v169, 24, v1
	v_and_b32_e32 v174, 4, v18
	s_cmpk_gt_i32 s21, 0x13ff
	v_add_u32_e32 v170, v3, v4
	v_add_u32_e32 v171, v6, v5
	s_cbranch_scc1 .LBB0_115
	v_mov_b32_e32 v3, 0
	s_load_dwordx4 s[4:7], s[96:97], 0x38
	s_load_dwordx2 s[12:13], s[96:97], 0x48
	v_mov_b32_e32 v165, v3
	v_lshl_add_u64 v[8:9], s[94:95], 0, v[164:165]
	s_mov_b64 s[16:17], 0x3e00000
	v_lshl_add_u64 v[4:5], v[8:9], 0, s[16:17]
	s_mov_b64 s[16:17], 0x3600000
	v_lshlrev_b32_e32 v20, 2, v2
	v_lshlrev_b32_e32 v2, 3, v2
	v_lshl_add_u64 v[6:7], v[8:9], 0, s[16:17]
	s_mov_b64 s[16:17], 0x3200000
	v_lshlrev_b32_e32 v21, 14, v1
	v_and_or_b32 v22, v2, 24, v174
	v_lshlrev_b32_e32 v23, 1, v1
	v_lshl_add_u64 v[8:9], v[8:9], 0, s[16:17]
	v_lshl_or_b32 v24, s21, 6, v2
	s_lshl_b32 s22, s20, 6
	s_lshl_b32 s23, s21, 5
	s_lshl_b32 s24, s20, 5
	s_movk_i32 s25, 0x2000
	s_mov_b32 s26, 0x20000
	s_mov_b32 s27, 0x22000
	s_mov_b32 s28, 0x40000
	s_mov_b32 s29, 0x42000
	s_mov_b32 s30, 0x60000
	s_mov_b32 s31, 0x62000
	v_add_u32_e32 v25, 0x420, v171
	v_add_u32_e32 v26, 0x428, v171
	v_add_u32_e32 v27, 0x840, v171
	v_add_u32_e32 v28, 0x848, v171
	v_add_u32_e32 v29, 0xc60, v171
	s_waitcnt vmcnt(1)
	v_add_u32_e32 v30, 0xc68, v171
	s_mov_b32 s33, s21
	s_branch .LBB0_107

;     __device__ __forceinline__ bool next(int i, Unit& u) const {
;         const long L = (long)i * G + c; if (L >= nwg) return false;
;         int wgid = (int)L; { const int q = nwg / NXCD, r = nwg % NXCD, xcd = wgid % NXCD, off = wgid / NXCD; wgid = (xcd < r ? xcd * (q + 1) : r * (q + 1) + (xcd - r) * q) + off; }
;         const int nig = WGM * nN, gid = wgid / nig, fm = gid * WGM, gsz = (nM - fm) < WGM ? (nM - fm) : WGM;
;         u.pm = fm + ((wgid % nig) % gsz); u.pn = (wgid % nig) / gsz; u.e = 0; u.mt = u.pm; u.hx = 0; return true;
;     }
;     int sclw = SCW * 0x01010101, scla = SCA * 0x01010101; asm volatile("" : "+v"(sclw), "+v"(scla));
;     int tid_ = threadIdx.x; asm volatile("" : "+v"(tid_));
;     const int tid = tid_, wid = __builtin_amdgcn_readfirstlane(tid >> 6), lane = tid & 63, wr = wid >> 2, wc = wid & 3, fr = lane & 15, fq = lane >> 4;
.Lgemm_entry:
	v_mov_b32_e32 v1, 0x7f7f7f7f
	s_waitcnt vmcnt(2)
	v_mov_b32_e32 v2, 0x7f7f7f7f
	s_cmpk_lt_i32 s92, 0xc00
	v_mov_b32_e32 v2, v0
	s_cselect_b64 s[0:1], -1, 0
	v_readfirstlane_b32 s4, v2
	s_ashr_i32 s6, s4, 6
	s_cmpk_gt_i32 s92, 0xbff
	s_cbranch_scc1 .LBB0_129
	s_ashr_i32 s5, s92, 31
	s_lshr_b32 s5, s5, 29
	s_add_i32 s5, s92, s5
	s_ashr_i32 s7, s5, 3
	s_and_b32 s5, s5, -8
	s_sub_i32 s5, s92, s5
	s_cmp_lt_i32 s5, 0
	s_movk_i32 s8, 0x181
	s_cselect_b32 s8, s8, 0x180
	s_mul_i32 s5, s5, s8
	s_add_i32 s5, s5, s7
	s_mul_hi_i32 s7, s5, 0x2aaaaaab
	s_lshr_b32 s8, s7, 31
	s_ashr_i32 s7, s7, 5
	s_add_i32 s7, s7, s8
	s_lshl_b32 s8, s7, 2
	s_mulk_i32 s7, 0xc0
	s_sub_i32 s5, s5, s7
	s_sext_i32_i16 s7, s5
	s_bfe_u32 s7, s7, 0x2001d
	s_add_i32 s7, s5, s7
	s_sext_i32_i16 s9, s7
	s_and_b32 s7, s7, 0xfffc
	s_sub_i32 s5, s5, s7
	s_sext_i32_i16 s5, s5
	s_add_i32 s10, s8, s5
	s_ashr_i32 s52, s9, 2

; #define SEAM(k) do { if (IN(k) && IN((k) + 1)) xcd_barrier(bar); } while (0)
; #define REPBAR(k) do { if ((((MK_DUP) >> (k)) & 1) && rep_ == 0) xcd_barrier(bar); } while (0)
; __global__ void __launch_bounds__(NTHREADS, 2) mk_fwd(Args args) {
;     ...
;         } else if (!MK_CONV_IN_P0) conv_rest(F, args, ((int)blockIdx.x - ngemm) * NWAVES + F.wave, nconv * NWAVES);
;         REPBAR(1);
;     } SEAM(1);
.LBB0_282:
	s_cmp_eq_u32 s101, 0
	s_cbranch_scc1 .Ldefer_norm
	s_mov_b32 s101, 0
	s_mov_b32 s92, s98
	s_ashr_i32 s93, s92, 31
	s_mov_b64 s[0:1], -1
	s_branch .LBB0_412

; #define SEAM(k) do { if (IN(k) && IN((k) + 1)) xcd_barrier(bar); } while (0)
; #define REP(k) for (int rep_ = reframe(F); rep_ < (((MK_DUP) >> (k)) & 1) + 1; ++rep_)
; #define REPBAR(k) do { if ((((MK_DUP) >> (k)) & 1) && rep_ == 0) xcd_barrier(bar); } while (0)
; __device__ __forceinline__ void scan_phase(Frame& F, const Args& a, int bi, int nb) {
;     const unsigned* KV = (const unsigned*)(F.ws + WS_KV); unsigned* ST = (unsigned*)(F.ws + WS_ST);
;     for (int pb = bi * NTHREADS; pb < 131072; pb += nb * NTHREADS) {
;         const int h = __builtin_amdgcn_readfirstlane(pb >> 14); const unsigned qo = (unsigned)(pb & 16383) + (unsigned)F.tid; const float dh = exp2f(128.0f * a.l2g[h]);
;         const unsigned* kvb = KV + (size_t)h * 16384; unsigned* stb = ST + (size_t)h * 16384;
;         float s0 = 0.f, s1 = 0.f;
;         {
;             unsigned kv[NCHUNK];
; #pragma unroll
;             for (int j = 0; j < NCHUNK; ++j) kv[j] = __builtin_nontemporal_load(kvb + (size_t)j * 131072 + qo);
; __global__ void __launch_bounds__(NTHREADS, 2) mk_fwd(Args args) {
;     ...
;     if (IN(3)) REP(3) {
;         const int nscan = (MK_NSCAN * F.G) / 256, nsp = F.G - nscan;
;         if (MK_NSCAN == 0) scan_phase(F, args, (int)blockIdx.x, F.G);
;         else if ((int)blockIdx.x < nsp) { for (int u = blockIdx.x; u < 1024; u += nsp) spatial_unit(F, args, u >> 3, u & 7); }
;         else scan_phase(F, args, (int)blockIdx.x - nsp, nscan);
;         REPBAR(3);
;     } SEAM(3);
.LBB0_407:
	s_cmp_lt_i32 s88, 4
	s_cselect_b64 s[4:5], -1, 0
	s_and_b64 s[0:1], s[4:5], s[0:1]
	s_andn2_b64 vcc, exec, s[0:1]
	s_cbranch_vccnz .LBB0_412
	v_mov_b32_e32 v1, v0
	s_cmpk_gt_i32 s92, 0xff
	s_cbranch_scc1 .LBB0_412
	s_cmpk_lt_i32 s92, 0x80
	s_cbranch_scc1 .Lp3_scan
	s_cmpk_ge_i32 s92, 0x100
	s_cbranch_scc1 .Lp3_idle
	s_add_i32 s92, s92, 0xb00
	s_movk_i32 s3, 128
	s_movk_i32 s99, 0xc00
	s_mov_b32 s101, 1
	s_branch .Lgemm_entry
.Lp3_idle:
	s_mov_b64 s[0:1], -1
	s_branch .LBB0_412
.Lp3_scan:
	v_writelane_b32 v254, s0, 14
	s_waitcnt vmcnt(1)
	v_mov_b32_e32 v8, 0x43000000
	v_mov_b32_e32 v3, 0
	v_writelane_b32 v254, s1, 15
	s_add_u32 s0, s94, 0x53000000
	v_writelane_b32 v254, s0, 16
	s_addc_u32 s0, s95, 0
	v_writelane_b32 v254, s0, 18
	s_add_u32 s0, s94, 0x5b000000
	v_writelane_b32 v254, s0, 20
	s_addc_u32 s0, s95, 0
	v_writelane_b32 v254, s0, 22
	s_mov_b32 s0, s2
	v_writelane_b32 v254, s0, 24
	s_lshl_b32 s10, s92, 9
	v_mov_b32_e32 v9, 0x42800000
	v_writelane_b32 v254, s1, 25
	s_mov_b32 s0, 0x10000
	v_writelane_b32 v254, s0, 26
	s_mov_b32 s0, s92
	v_writelane_b32 v254, s0, 12
	s_mov_b32 s55, 0x80000
	s_mov_b32 s56, 0x100000
	v_writelane_b32 v254, s1, 13
	v_writelane_b32 v254, s96, 10
	s_mov_b32 s57, 0x180000
	s_mov_b32 s58, 0x200000
	v_writelane_b32 v254, s97, 11
	s_mov_b32 s59, 0x280000
	s_mov_b32 s60, 0x300000
	s_mov_b32 s61, 0x380000
	s_mov_b32 s62, 0x400000
	s_mov_b32 s63, 0x480000
	s_mov_b32 s64, 0x500000
	s_mov_b32 s65, 0x580000
	s_mov_b32 s66, 0x600000
	s_mov_b32 s67, 0x680000
	s_mov_b32 s68, 0x700000
	s_mov_b32 s69, 0x780000
	s_mov_b32 s70, 0x800000
	s_mov_b32 s71, 0x880000
	s_mov_b32 s72, 0x900000
	s_mov_b32 s73, 0x980000
	s_mov_b32 s74, 0xa00000
	s_mov_b32 s75, 0xa80000
	s_mov_b32 s76, 0xb00000
	s_mov_b32 s77, 0xb80000
	s_mov_b32 s78, 0xc00000
	s_mov_b32 s79, 0xc80000
	s_mov_b32 s80, 0xd00000
	s_mov_b32 s81, 0xd80000
	s_mov_b32 s82, 0xe00000
	s_mov_b32 s83, 0xe80000
	s_mov_b32 s84, 0xf00000
	s_mov_b32 s85, 0xf80000
	s_mov_b32 s86, 0x1000000
	s_mov_b32 s87, 0x1080000
	s_mov_b32 s88, 0x1100000
	s_mov_b32 s89, 0x1180000
	s_mov_b32 s90, 0x1200000
	s_mov_b32 s91, 0x1280000
	s_mov_b32 s92, 0x1300000
	s_mov_b32 s93, 0x1380000
	s_mov_b32 s94, 0x1400000
	s_mov_b32 s95, 0x1480000
	s_mov_b32 s6, 0x1580000
	s_mov_b32 s7, 0x1600000
	s_mov_b32 s8, 0x1680000
	s_mov_b32 s9, 0x1700000
	s_mov_b32 s53, 0x1780000
	s_mov_b32 s54, 0x1800000
	s_mov_b32 s33, 0x1880000
	s_mov_b32 s11, 0x1a00000
	s_mov_b32 s12, 0x1a80000
	s_mov_b32 s13, 0x1b00000
	s_mov_b32 s14, 0x1b80000
	s_mov_b32 s15, 0x1c00000
	s_mov_b32 s16, 0x1c80000
	s_mov_b32 s17, 0x1d00000
	s_mov_b32 s18, 0x1d80000
	s_mov_b32 s19, 0x1e00000
	s_mov_b32 s20, 0x1e80000
	s_mov_b32 s21, 0x1f00000
	s_mov_b32 s22, 0x1f80000
	s_brev_b32 s23, 64
	s_mov_b32 s24, 0x2080000
	s_mov_b32 s25, 0x2100000
	s_mov_b32 s26, 0x2180000
	s_mov_b32 s27, 0x2200000
	s_mov_b32 s28, 0x2280000
	s_mov_b32 s29, 0x2300000
	s_mov_b32 s30, 0x2380000
	s_mov_b32 s31, 0x2400000
	s_mov_b32 s34, 0x2480000
	s_mov_b32 s35, 0x2500000
	s_mov_b32 s36, 0x2580000
	s_mov_b32 s37, 0x2600000
	s_mov_b32 s38, 0x2680000
	s_mov_b32 s39, 0x2700000
	s_mov_b32 s40, 0x2780000
	s_mov_b32 s41, 0x2800000
	s_mov_b32 s42, 0x2880000
	s_mov_b32 s43, 0x2900000
	s_mov_b32 s44, 0x2980000
	s_mov_b32 s45, 0x2a00000
	s_mov_b32 s46, 0x2a80000
	s_mov_b32 s47, 0x2b00000
	s_mov_b32 s48, 0x2b80000
	s_mov_b32 s49, 0x2c00000
	s_mov_b32 s50, 0x2c80000
	s_mov_b32 s2, 0x2d00000
	s_mov_b32 s96, 0x2d80000
	s_mov_b32 s97, 0x2e00000
